# v29: v21 + code placement: each GEMM K-loop head at the 8-byte phase that leaves the fewest MFMAs straddling an 8-byte boundary
# baseline (speedup 1.0000x reference)
.LBB0_243:
	s_add_u32 s0, s40, 0x100
	v_mov_b32_e32 v2, 0
	s_addc_u32 s1, s41, 0
	s_mov_b32 s3, -2
	v_mov_b32_e32 v3, v2
	v_mov_b32_e32 v4, v2
	v_mov_b32_e32 v5, v2
	v_mov_b32_e32 v6, v2
	v_mov_b32_e32 v7, v2
	v_mov_b32_e32 v8, v2
	v_mov_b32_e32 v9, v2
	v_mov_b32_e32 v18, v2
	v_mov_b32_e32 v19, v2
	v_mov_b32_e32 v20, v2
	v_mov_b32_e32 v21, v2
	v_mov_b32_e32 v22, v2
	v_mov_b32_e32 v23, v2
	v_mov_b32_e32 v24, v2
	v_mov_b32_e32 v25, v2
	s_waitcnt vmcnt(0)
	v_mov_b32_e32 v34, v2
	v_mov_b32_e32 v35, v2
	v_mov_b32_e32 v36, v2
	v_mov_b32_e32 v37, v2
	v_mov_b32_e32 v38, v2
	v_mov_b32_e32 v39, v2
	v_mov_b32_e32 v40, v2
	v_mov_b32_e32 v41, v2
	v_mov_b32_e32 v50, v2
	v_mov_b32_e32 v51, v2
	v_mov_b32_e32 v52, v2
	v_mov_b32_e32 v53, v2
	v_mov_b32_e32 v54, v2
	v_mov_b32_e32 v55, v2
	v_mov_b32_e32 v56, v2
	v_mov_b32_e32 v57, v2
	v_mov_b32_e32 v82, v2
	v_mov_b32_e32 v83, v2
	v_mov_b32_e32 v84, v2
	v_mov_b32_e32 v85, v2
	v_mov_b32_e32 v86, v2
	v_mov_b32_e32 v87, v2
	v_mov_b32_e32 v88, v2
	v_mov_b32_e32 v89, v2
	v_mov_b32_e32 v102, v2
	v_mov_b32_e32 v103, v2
	v_mov_b32_e32 v104, v2
	v_mov_b32_e32 v105, v2
	v_mov_b32_e32 v106, v2
	v_mov_b32_e32 v107, v2
	v_mov_b32_e32 v108, v2
	v_mov_b32_e32 v109, v2
	v_mov_b32_e32 v122, v2
	v_mov_b32_e32 v123, v2
	v_mov_b32_e32 v124, v2
	v_mov_b32_e32 v125, v2
	v_mov_b32_e32 v126, v2
	v_mov_b32_e32 v127, v2
	v_mov_b32_e32 v128, v2
	v_mov_b32_e32 v129, v2
	v_mov_b32_e32 v150, v2
	v_mov_b32_e32 v151, v2
	v_mov_b32_e32 v152, v2
	v_mov_b32_e32 v153, v2
	v_mov_b32_e32 v154, v2
	v_mov_b32_e32 v155, v2
	v_mov_b32_e32 v156, v2
	v_mov_b32_e32 v157, v2
	v_mov_b32_e32 v90, v2
	v_mov_b32_e32 v91, v2
	v_mov_b32_e32 v92, v2
	v_mov_b32_e32 v93, v2
	v_mov_b32_e32 v94, v2
	v_mov_b32_e32 v95, v2
	v_mov_b32_e32 v96, v2
	v_mov_b32_e32 v97, v2
	v_mov_b32_e32 v110, v2
	v_mov_b32_e32 v111, v2
	v_mov_b32_e32 v112, v2
	v_mov_b32_e32 v113, v2
	v_mov_b32_e32 v114, v2
	v_mov_b32_e32 v115, v2
	v_mov_b32_e32 v116, v2
	v_mov_b32_e32 v117, v2
	v_mov_b32_e32 v130, v2
	v_mov_b32_e32 v131, v2
	v_mov_b32_e32 v132, v2
	v_mov_b32_e32 v133, v2
	v_mov_b32_e32 v134, v2
	v_mov_b32_e32 v135, v2
	v_mov_b32_e32 v136, v2
	v_mov_b32_e32 v137, v2
	v_mov_b32_e32 v158, v2
	v_mov_b32_e32 v159, v2
	v_mov_b32_e32 v160, v2
	v_mov_b32_e32 v161, v2
	v_mov_b32_e32 v162, v2
	v_mov_b32_e32 v163, v2
	v_mov_b32_e32 v164, v2
	v_mov_b32_e32 v165, v2
	v_mov_b32_e32 v58, v2
	v_mov_b32_e32 v59, v2
	v_mov_b32_e32 v60, v2
	v_mov_b32_e32 v61, v2
	v_mov_b32_e32 v62, v2
	v_mov_b32_e32 v63, v2
	v_mov_b32_e32 v64, v2
	v_mov_b32_e32 v65, v2
	v_mov_b32_e32 v42, v2
	v_mov_b32_e32 v43, v2
	v_mov_b32_e32 v44, v2
	v_mov_b32_e32 v45, v2
	v_mov_b32_e32 v46, v2
	v_mov_b32_e32 v47, v2
	v_mov_b32_e32 v48, v2
	v_mov_b32_e32 v49, v2
	v_mov_b32_e32 v26, v2
	v_mov_b32_e32 v27, v2
	v_mov_b32_e32 v28, v2
	v_mov_b32_e32 v29, v2
	v_mov_b32_e32 v30, v2
	v_mov_b32_e32 v31, v2
	v_mov_b32_e32 v32, v2
	v_mov_b32_e32 v33, v2
	v_mov_b32_e32 v10, v2
	v_mov_b32_e32 v11, v2
	v_mov_b32_e32 v12, v2
	v_mov_b32_e32 v13, v2
	v_mov_b32_e32 v14, v2
	v_mov_b32_e32 v15, v2
	s_waitcnt lgkmcnt(0)
	v_mov_b32_e32 v16, v2
	v_mov_b32_e32 v17, v2
	.p2align	3
	s_nop 0

.LBB0_450:
	s_add_u32 s5, s46, 0x100
	s_addc_u32 s16, s47, 0
	s_add_u32 s17, s2, 0x100
	s_addc_u32 s18, s3, 0
	s_add_u32 s2, s2, 0x80
	s_addc_u32 s3, s3, 0
	s_mov_b32 s19, -2
	.p2align	3

.LBB0_563:
	s_add_u32 s0, s22, 0x100
	v_mov_b32_e32 v2, 0
	s_addc_u32 s1, s23, 0
	s_mov_b32 s13, -2
	s_waitcnt lgkmcnt(0)
	v_mov_b32_e32 v3, v2
	v_mov_b32_e32 v4, v2
	v_mov_b32_e32 v5, v2
	v_mov_b32_e32 v6, v2
	v_mov_b32_e32 v7, v2
	v_mov_b32_e32 v8, v2
	v_mov_b32_e32 v9, v2
	v_mov_b32_e32 v18, v2
	v_mov_b32_e32 v19, v2
	v_mov_b32_e32 v20, v2
	v_mov_b32_e32 v21, v2
	v_mov_b32_e32 v22, v2
	v_mov_b32_e32 v23, v2
	v_mov_b32_e32 v24, v2
	v_mov_b32_e32 v25, v2
	v_mov_b32_e32 v50, v2
	v_mov_b32_e32 v51, v2
	v_mov_b32_e32 v52, v2
	v_mov_b32_e32 v53, v2
	v_mov_b32_e32 v54, v2
	v_mov_b32_e32 v55, v2
	v_mov_b32_e32 v56, v2
	v_mov_b32_e32 v57, v2
	v_mov_b32_e32 v82, v2
	v_mov_b32_e32 v83, v2
	v_mov_b32_e32 v84, v2
	v_mov_b32_e32 v85, v2
	s_waitcnt vmcnt(1)
	v_mov_b32_e32 v86, v2
	v_mov_b32_e32 v87, v2
	v_mov_b32_e32 v88, v2
	v_mov_b32_e32 v89, v2
	v_mov_b32_e32 v98, v2
	v_mov_b32_e32 v99, v2
	v_mov_b32_e32 v100, v2
	v_mov_b32_e32 v101, v2
	v_mov_b32_e32 v102, v2
	v_mov_b32_e32 v103, v2
	v_mov_b32_e32 v104, v2
	v_mov_b32_e32 v105, v2
	v_mov_b32_e32 v114, v2
	v_mov_b32_e32 v115, v2
	v_mov_b32_e32 v116, v2
	v_mov_b32_e32 v117, v2
	v_mov_b32_e32 v118, v2
	v_mov_b32_e32 v119, v2
	v_mov_b32_e32 v120, v2
	v_mov_b32_e32 v121, v2
	v_mov_b32_e32 v130, v2
	v_mov_b32_e32 v131, v2
	v_mov_b32_e32 v132, v2
	v_mov_b32_e32 v133, v2
	s_waitcnt vmcnt(0)
	v_mov_b32_e32 v134, v2
	v_mov_b32_e32 v135, v2
	v_mov_b32_e32 v136, v2
	v_mov_b32_e32 v137, v2
	v_mov_b32_e32 v146, v2
	v_mov_b32_e32 v147, v2
	v_mov_b32_e32 v148, v2
	v_mov_b32_e32 v149, v2
	v_mov_b32_e32 v150, v2
	v_mov_b32_e32 v151, v2
	v_mov_b32_e32 v152, v2
	v_mov_b32_e32 v153, v2
	v_mov_b32_e32 v106, v2
	v_mov_b32_e32 v107, v2
	v_mov_b32_e32 v108, v2
	v_mov_b32_e32 v109, v2
	v_mov_b32_e32 v110, v2
	v_mov_b32_e32 v111, v2
	v_mov_b32_e32 v112, v2
	v_mov_b32_e32 v113, v2
	v_mov_b32_e32 v122, v2
	v_mov_b32_e32 v123, v2
	v_mov_b32_e32 v124, v2
	v_mov_b32_e32 v125, v2
	v_mov_b32_e32 v126, v2
	v_mov_b32_e32 v127, v2
	v_mov_b32_e32 v128, v2
	v_mov_b32_e32 v129, v2
	v_mov_b32_e32 v138, v2
	v_mov_b32_e32 v139, v2
	v_mov_b32_e32 v140, v2
	v_mov_b32_e32 v141, v2
	v_mov_b32_e32 v142, v2
	v_mov_b32_e32 v143, v2
	v_mov_b32_e32 v144, v2
	v_mov_b32_e32 v145, v2
	v_mov_b32_e32 v154, v2
	v_mov_b32_e32 v155, v2
	v_mov_b32_e32 v156, v2
	v_mov_b32_e32 v157, v2
	v_mov_b32_e32 v158, v2
	v_mov_b32_e32 v159, v2
	v_mov_b32_e32 v160, v2
	v_mov_b32_e32 v161, v2
	v_mov_b32_e32 v90, v2
	v_mov_b32_e32 v91, v2
	v_mov_b32_e32 v92, v2
	v_mov_b32_e32 v93, v2
	v_mov_b32_e32 v94, v2
	v_mov_b32_e32 v95, v2
	v_mov_b32_e32 v96, v2
	v_mov_b32_e32 v97, v2
	v_mov_b32_e32 v58, v2
	v_mov_b32_e32 v59, v2
	v_mov_b32_e32 v60, v2
	v_mov_b32_e32 v61, v2
	v_mov_b32_e32 v62, v2
	v_mov_b32_e32 v63, v2
	v_mov_b32_e32 v64, v2
	v_mov_b32_e32 v65, v2
	v_mov_b32_e32 v26, v2
	v_mov_b32_e32 v27, v2
	v_mov_b32_e32 v28, v2
	v_mov_b32_e32 v29, v2
	v_mov_b32_e32 v30, v2
	v_mov_b32_e32 v31, v2
	v_mov_b32_e32 v32, v2
	v_mov_b32_e32 v33, v2
	v_mov_b32_e32 v10, v2
	v_mov_b32_e32 v11, v2
	v_mov_b32_e32 v12, v2
	v_mov_b32_e32 v13, v2
	v_mov_b32_e32 v14, v2
	v_mov_b32_e32 v15, v2
	s_waitcnt lgkmcnt(0)
	v_mov_b32_e32 v16, v2
	v_mov_b32_e32 v17, v2
	.p2align	3
	s_nop 0

.LBB0_792:
	s_add_u32 s0, s22, 0x100
	v_mov_b32_e32 v2, 0
	s_addc_u32 s1, s23, 0
	s_mov_b32 s5, -2
	v_mov_b32_e32 v3, v2
	v_mov_b32_e32 v4, v2
	v_mov_b32_e32 v5, v2
	v_mov_b32_e32 v6, v2
	v_mov_b32_e32 v7, v2
	v_mov_b32_e32 v8, v2
	v_mov_b32_e32 v9, v2
	v_mov_b32_e32 v18, v2
	v_mov_b32_e32 v19, v2
	v_mov_b32_e32 v20, v2
	v_mov_b32_e32 v21, v2
	v_mov_b32_e32 v22, v2
	v_mov_b32_e32 v23, v2
	v_mov_b32_e32 v24, v2
	v_mov_b32_e32 v25, v2
	s_waitcnt vmcnt(0)
	v_mov_b32_e32 v34, v2
	v_mov_b32_e32 v35, v2
	v_mov_b32_e32 v36, v2
	v_mov_b32_e32 v37, v2
	v_mov_b32_e32 v38, v2
	v_mov_b32_e32 v39, v2
	v_mov_b32_e32 v40, v2
	v_mov_b32_e32 v41, v2
	v_mov_b32_e32 v50, v2
	v_mov_b32_e32 v51, v2
	v_mov_b32_e32 v52, v2
	v_mov_b32_e32 v53, v2
	v_mov_b32_e32 v54, v2
	v_mov_b32_e32 v55, v2
	v_mov_b32_e32 v56, v2
	v_mov_b32_e32 v57, v2
	v_mov_b32_e32 v66, v2
	v_mov_b32_e32 v67, v2
	v_mov_b32_e32 v68, v2
	v_mov_b32_e32 v69, v2
	v_mov_b32_e32 v70, v2
	v_mov_b32_e32 v71, v2
	v_mov_b32_e32 v72, v2
	v_mov_b32_e32 v73, v2
	v_mov_b32_e32 v106, v2
	v_mov_b32_e32 v107, v2
	v_mov_b32_e32 v108, v2
	v_mov_b32_e32 v109, v2
	v_mov_b32_e32 v114, v2
	v_mov_b32_e32 v115, v2
	v_mov_b32_e32 v116, v2
	v_mov_b32_e32 v117, v2
	v_mov_b32_e32 v146, v2
	v_mov_b32_e32 v147, v2
	v_mov_b32_e32 v148, v2
	v_mov_b32_e32 v149, v2
	v_mov_b32_e32 v150, v2
	v_mov_b32_e32 v151, v2
	v_mov_b32_e32 v152, v2
	v_mov_b32_e32 v153, v2
	v_mov_b32_e32 v178, v2
	v_mov_b32_e32 v179, v2
	v_mov_b32_e32 v180, v2
	v_mov_b32_e32 v181, v2
	v_mov_b32_e32 v182, v2
	v_mov_b32_e32 v183, v2
	v_mov_b32_e32 v184, v2
	v_mov_b32_e32 v185, v2
	v_mov_b32_e32 v78, v2
	v_mov_b32_e32 v79, v2
	v_mov_b32_e32 v80, v2
	v_mov_b32_e32 v81, v2
	v_mov_b32_e32 v82, v2
	v_mov_b32_e32 v83, v2
	v_mov_b32_e32 v84, v2
	v_mov_b32_e32 v85, v2
	v_mov_b32_e32 v122, v2
	v_mov_b32_e32 v123, v2
	v_mov_b32_e32 v124, v2
	v_mov_b32_e32 v125, v2
	v_mov_b32_e32 v126, v2
	v_mov_b32_e32 v127, v2
	v_mov_b32_e32 v128, v2
	v_mov_b32_e32 v129, v2
	v_mov_b32_e32 v154, v2
	v_mov_b32_e32 v155, v2
	v_mov_b32_e32 v156, v2
	v_mov_b32_e32 v157, v2
	v_mov_b32_e32 v158, v2
	v_mov_b32_e32 v159, v2
	v_mov_b32_e32 v160, v2
	v_mov_b32_e32 v161, v2
	v_mov_b32_e32 v186, v2
	v_mov_b32_e32 v187, v2
	v_mov_b32_e32 v188, v2
	v_mov_b32_e32 v189, v2
	v_mov_b32_e32 v190, v2
	v_mov_b32_e32 v191, v2
	v_mov_b32_e32 v192, v2
	v_mov_b32_e32 v193, v2
	v_mov_b32_e32 v58, v2
	v_mov_b32_e32 v59, v2
	v_mov_b32_e32 v60, v2
	v_mov_b32_e32 v61, v2
	v_mov_b32_e32 v62, v2
	v_mov_b32_e32 v63, v2
	v_mov_b32_e32 v64, v2
	v_mov_b32_e32 v65, v2
	v_mov_b32_e32 v42, v2
	v_mov_b32_e32 v43, v2
	v_mov_b32_e32 v44, v2
	v_mov_b32_e32 v45, v2
	v_mov_b32_e32 v46, v2
	v_mov_b32_e32 v47, v2
	v_mov_b32_e32 v48, v2
	v_mov_b32_e32 v49, v2
	v_mov_b32_e32 v26, v2
	v_mov_b32_e32 v27, v2
	v_mov_b32_e32 v28, v2
	v_mov_b32_e32 v29, v2
	v_mov_b32_e32 v30, v2
	v_mov_b32_e32 v31, v2
	v_mov_b32_e32 v32, v2
	v_mov_b32_e32 v33, v2
	v_mov_b32_e32 v10, v2
	v_mov_b32_e32 v11, v2
	v_mov_b32_e32 v12, v2
	v_mov_b32_e32 v13, v2
	v_mov_b32_e32 v14, v2
	v_mov_b32_e32 v15, v2
	v_mov_b32_e32 v16, v2
	v_mov_b32_e32 v17, v2
	.p2align	3
	s_nop 0

.LBB0_856:
	s_waitcnt vmcnt(7)
	v_mov_b32_e32 v66, 0
	s_mov_b64 s[50:51], 0
	s_mov_b64 s[46:47], -1
	s_mov_b64 s[48:49], 0
	v_mov_b32_e32 v67, v66
	v_mov_b32_e32 v68, v66
	v_mov_b32_e32 v69, v66
	s_waitcnt vmcnt(4)
	v_mov_b32_e32 v70, v66
	v_mov_b32_e32 v71, v66
	v_mov_b32_e32 v72, v66
	v_mov_b32_e32 v73, v66
	v_mov_b32_e32 v82, v66
	v_mov_b32_e32 v83, v66
	v_mov_b32_e32 v84, v66
	v_mov_b32_e32 v85, v66
	s_waitcnt vmcnt(1)
	v_mov_b32_e32 v86, v66
	v_mov_b32_e32 v87, v66
	v_mov_b32_e32 v88, v66
	v_mov_b32_e32 v89, v66
	v_mov_b32_e32 v98, v66
	v_mov_b32_e32 v99, v66
	v_mov_b32_e32 v100, v66
	v_mov_b32_e32 v101, v66
	v_mov_b32_e32 v102, v66
	v_mov_b32_e32 v103, v66
	v_mov_b32_e32 v104, v66
	v_mov_b32_e32 v105, v66
	v_mov_b32_e32 v114, v66
	v_mov_b32_e32 v115, v66
	v_mov_b32_e32 v116, v66
	v_mov_b32_e32 v117, v66
	v_mov_b32_e32 v118, v66
	v_mov_b32_e32 v119, v66
	v_mov_b32_e32 v120, v66
	v_mov_b32_e32 v121, v66
	v_mov_b32_e32 v130, v66
	v_mov_b32_e32 v131, v66
	v_mov_b32_e32 v132, v66
	v_mov_b32_e32 v133, v66
	s_waitcnt vmcnt(0)
	v_mov_b32_e32 v134, v66
	v_mov_b32_e32 v135, v66
	v_mov_b32_e32 v136, v66
	v_mov_b32_e32 v137, v66
	v_mov_b32_e32 v146, v66
	v_mov_b32_e32 v147, v66
	v_mov_b32_e32 v148, v66
	v_mov_b32_e32 v149, v66
	v_mov_b32_e32 v150, v66
	v_mov_b32_e32 v151, v66
	v_mov_b32_e32 v152, v66
	v_mov_b32_e32 v153, v66
	v_mov_b32_e32 v162, v66
	v_mov_b32_e32 v163, v66
	v_mov_b32_e32 v164, v66
	v_mov_b32_e32 v165, v66
	v_mov_b32_e32 v166, v66
	v_mov_b32_e32 v167, v66
	v_mov_b32_e32 v168, v66
	v_mov_b32_e32 v169, v66
	v_mov_b32_e32 v178, v66
	v_mov_b32_e32 v179, v66
	v_mov_b32_e32 v180, v66
	v_mov_b32_e32 v181, v66
	v_mov_b32_e32 v182, v66
	v_mov_b32_e32 v183, v66
	v_mov_b32_e32 v184, v66
	v_mov_b32_e32 v185, v66
	v_mov_b32_e32 v138, v66
	v_mov_b32_e32 v139, v66
	v_mov_b32_e32 v140, v66
	v_mov_b32_e32 v141, v66
	v_mov_b32_e32 v142, v66
	v_mov_b32_e32 v143, v66
	v_mov_b32_e32 v144, v66
	v_mov_b32_e32 v145, v66
	v_mov_b32_e32 v154, v66
	v_mov_b32_e32 v155, v66
	v_mov_b32_e32 v156, v66
	v_mov_b32_e32 v157, v66
	v_mov_b32_e32 v158, v66
	v_mov_b32_e32 v159, v66
	v_mov_b32_e32 v160, v66
	v_mov_b32_e32 v161, v66
	v_mov_b32_e32 v170, v66
	v_mov_b32_e32 v171, v66
	v_mov_b32_e32 v172, v66
	v_mov_b32_e32 v173, v66
	v_mov_b32_e32 v174, v66
	v_mov_b32_e32 v175, v66
	v_mov_b32_e32 v176, v66
	v_mov_b32_e32 v177, v66
	v_mov_b32_e32 v186, v66
	v_mov_b32_e32 v187, v66
	v_mov_b32_e32 v188, v66
	v_mov_b32_e32 v189, v66
	v_mov_b32_e32 v190, v66
	v_mov_b32_e32 v191, v66
	v_mov_b32_e32 v192, v66
	v_mov_b32_e32 v193, v66
	v_mov_b32_e32 v122, v66
	v_mov_b32_e32 v123, v66
	v_mov_b32_e32 v124, v66
	v_mov_b32_e32 v125, v66
	v_mov_b32_e32 v126, v66
	v_mov_b32_e32 v127, v66
	v_mov_b32_e32 v128, v66
	v_mov_b32_e32 v129, v66
	v_mov_b32_e32 v106, v66
	v_mov_b32_e32 v107, v66
	v_mov_b32_e32 v108, v66
	v_mov_b32_e32 v109, v66
	v_mov_b32_e32 v110, v66
	v_mov_b32_e32 v111, v66
	v_mov_b32_e32 v112, v66
	v_mov_b32_e32 v113, v66
	s_waitcnt vmcnt(0)
	v_mov_b32_e32 v90, v66
	v_mov_b32_e32 v91, v66
	v_mov_b32_e32 v92, v66
	v_mov_b32_e32 v93, v66
	v_mov_b32_e32 v94, v66
	v_mov_b32_e32 v95, v66
	v_mov_b32_e32 v96, v66
	v_mov_b32_e32 v97, v66
	v_mov_b32_e32 v74, v66
	v_mov_b32_e32 v75, v66
	v_mov_b32_e32 v76, v66
	v_mov_b32_e32 v77, v66
	v_mov_b32_e32 v78, v66
	v_mov_b32_e32 v79, v66
	v_mov_b32_e32 v80, v66
	v_mov_b32_e32 v81, v66
	.p2align	3
	s_nop 0

.LBB0_1160:
	s_add_u32 s5, s44, 0x100
	s_addc_u32 s16, s45, 0
	s_add_u32 s17, s42, 0x100
	s_addc_u32 s18, s43, 0
	s_add_u32 s42, s42, 0x80
	s_addc_u32 s43, s43, 0
	s_mov_b32 s19, -2
	.p2align	3

.LBB0_1728:
	s_add_u32 s16, s22, 0x100
	s_addc_u32 s17, s23, 0
	s_mov_b32 s18, -2
	s_mov_b64 s[56:57], s[30:31]
	.p2align	3

.LBB0_1814:
	s_add_u32 s18, s22, 0x100
	s_addc_u32 s19, s23, 0
	s_mov_b32 s21, -2
	.p2align	3
	s_nop 0

.LBB0_1938:
	s_add_u32 s0, s22, 0x100
	v_mov_b32_e32 v2, 0
	s_addc_u32 s1, s23, 0
	s_mov_b32 s3, -2
	v_mov_b32_e32 v3, v2
	v_mov_b32_e32 v4, v2
	v_mov_b32_e32 v5, v2
	v_mov_b32_e32 v10, v2
	v_mov_b32_e32 v11, v2
	v_mov_b32_e32 v12, v2
	v_mov_b32_e32 v13, v2
	v_mov_b32_e32 v18, v2
	v_mov_b32_e32 v19, v2
	v_mov_b32_e32 v20, v2
	v_mov_b32_e32 v21, v2
	v_mov_b32_e32 v26, v2
	v_mov_b32_e32 v27, v2
	v_mov_b32_e32 v28, v2
	v_mov_b32_e32 v29, v2
	s_waitcnt vmcnt(0)
	v_mov_b32_e32 v34, v2
	v_mov_b32_e32 v35, v2
	v_mov_b32_e32 v36, v2
	v_mov_b32_e32 v37, v2
	v_mov_b32_e32 v42, v2
	v_mov_b32_e32 v43, v2
	v_mov_b32_e32 v44, v2
	v_mov_b32_e32 v45, v2
	v_mov_b32_e32 v54, v2
	v_mov_b32_e32 v55, v2
	v_mov_b32_e32 v56, v2
	v_mov_b32_e32 v57, v2
	v_mov_b32_e32 v62, v2
	v_mov_b32_e32 v63, v2
	v_mov_b32_e32 v64, v2
	v_mov_b32_e32 v65, v2
	v_mov_b32_e32 v74, v2
	v_mov_b32_e32 v75, v2
	v_mov_b32_e32 v76, v2
	v_mov_b32_e32 v77, v2
	v_mov_b32_e32 v82, v2
	v_mov_b32_e32 v83, v2
	v_mov_b32_e32 v84, v2
	v_mov_b32_e32 v85, v2
	v_mov_b32_e32 v94, v2
	v_mov_b32_e32 v95, v2
	v_mov_b32_e32 v96, v2
	v_mov_b32_e32 v97, v2
	v_mov_b32_e32 v102, v2
	v_mov_b32_e32 v103, v2
	v_mov_b32_e32 v104, v2
	v_mov_b32_e32 v105, v2
	v_mov_b32_e32 v114, v2
	v_mov_b32_e32 v115, v2
	v_mov_b32_e32 v116, v2
	v_mov_b32_e32 v117, v2
	v_mov_b32_e32 v122, v2
	v_mov_b32_e32 v123, v2
	v_mov_b32_e32 v124, v2
	v_mov_b32_e32 v125, v2
	v_mov_b32_e32 v138, v2
	v_mov_b32_e32 v139, v2
	v_mov_b32_e32 v140, v2
	v_mov_b32_e32 v141, v2
	v_mov_b32_e32 v146, v2
	v_mov_b32_e32 v147, v2
	v_mov_b32_e32 v148, v2
	v_mov_b32_e32 v149, v2
	v_mov_b32_e32 v78, v2
	v_mov_b32_e32 v79, v2
	v_mov_b32_e32 v80, v2
	v_mov_b32_e32 v81, v2
	v_mov_b32_e32 v86, v2
	v_mov_b32_e32 v87, v2
	v_mov_b32_e32 v88, v2
	v_mov_b32_e32 v89, v2
	v_mov_b32_e32 v98, v2
	v_mov_b32_e32 v99, v2
	v_mov_b32_e32 v100, v2
	v_mov_b32_e32 v101, v2
	v_mov_b32_e32 v106, v2
	v_mov_b32_e32 v107, v2
	v_mov_b32_e32 v108, v2
	v_mov_b32_e32 v109, v2
	v_mov_b32_e32 v118, v2
	v_mov_b32_e32 v119, v2
	v_mov_b32_e32 v120, v2
	v_mov_b32_e32 v121, v2
	v_mov_b32_e32 v126, v2
	v_mov_b32_e32 v127, v2
	v_mov_b32_e32 v128, v2
	v_mov_b32_e32 v129, v2
	v_mov_b32_e32 v142, v2
	v_mov_b32_e32 v143, v2
	v_mov_b32_e32 v144, v2
	v_mov_b32_e32 v145, v2
	v_mov_b32_e32 v150, v2
	v_mov_b32_e32 v151, v2
	v_mov_b32_e32 v152, v2
	v_mov_b32_e32 v153, v2
	v_mov_b32_e32 v66, v2
	v_mov_b32_e32 v67, v2
	v_mov_b32_e32 v68, v2
	v_mov_b32_e32 v69, v2
	v_mov_b32_e32 v58, v2
	v_mov_b32_e32 v59, v2
	v_mov_b32_e32 v60, v2
	v_mov_b32_e32 v61, v2
	v_mov_b32_e32 v46, v2
	v_mov_b32_e32 v47, v2
	v_mov_b32_e32 v48, v2
	v_mov_b32_e32 v49, v2
	v_mov_b32_e32 v38, v2
	v_mov_b32_e32 v39, v2
	v_mov_b32_e32 v40, v2
	v_mov_b32_e32 v41, v2
	v_mov_b32_e32 v30, v2
	v_mov_b32_e32 v31, v2
	v_mov_b32_e32 v32, v2
	v_mov_b32_e32 v33, v2
	v_mov_b32_e32 v22, v2
	v_mov_b32_e32 v23, v2
	v_mov_b32_e32 v24, v2
	v_mov_b32_e32 v25, v2
	v_mov_b32_e32 v14, v2
	v_mov_b32_e32 v15, v2
	v_mov_b32_e32 v16, v2
	v_mov_b32_e32 v17, v2
	v_mov_b32_e32 v6, v2
	v_mov_b32_e32 v7, v2
	v_mov_b32_e32 v8, v2
	v_mov_b32_e32 v9, v2
	.p2align	3
	s_nop 0

.LBB0_1958:
	s_add_u32 s5, s42, 0x100
	s_addc_u32 s13, s43, 0
	s_mov_b32 s17, -2
	.p2align	3

.LBB0_2034:
	s_add_u32 s0, s26, 0x100
	v_mov_b32_e32 v2, 0
	s_addc_u32 s1, s27, 0
	s_mov_b32 s5, -2
	s_waitcnt lgkmcnt(0)
	v_mov_b32_e32 v3, v2
	v_mov_b32_e32 v4, v2
	v_mov_b32_e32 v5, v2
	v_mov_b32_e32 v6, v2
	v_mov_b32_e32 v7, v2
	v_mov_b32_e32 v8, v2
	v_mov_b32_e32 v9, v2
	v_mov_b32_e32 v18, v2
	v_mov_b32_e32 v19, v2
	v_mov_b32_e32 v20, v2
	v_mov_b32_e32 v21, v2
	v_mov_b32_e32 v22, v2
	v_mov_b32_e32 v23, v2
	v_mov_b32_e32 v24, v2
	v_mov_b32_e32 v25, v2
	s_waitcnt vmcnt(0)
	v_mov_b32_e32 v34, v2
	v_mov_b32_e32 v35, v2
	v_mov_b32_e32 v36, v2
	v_mov_b32_e32 v37, v2
	v_mov_b32_e32 v38, v2
	v_mov_b32_e32 v39, v2
	v_mov_b32_e32 v40, v2
	v_mov_b32_e32 v41, v2
	v_mov_b32_e32 v50, v2
	v_mov_b32_e32 v51, v2
	v_mov_b32_e32 v52, v2
	v_mov_b32_e32 v53, v2
	v_mov_b32_e32 v54, v2
	v_mov_b32_e32 v55, v2
	v_mov_b32_e32 v56, v2
	v_mov_b32_e32 v57, v2
	v_mov_b32_e32 v66, v2
	v_mov_b32_e32 v67, v2
	v_mov_b32_e32 v68, v2
	v_mov_b32_e32 v69, v2
	v_mov_b32_e32 v70, v2
	v_mov_b32_e32 v71, v2
	v_mov_b32_e32 v72, v2
	v_mov_b32_e32 v73, v2
	v_mov_b32_e32 v82, v2
	v_mov_b32_e32 v83, v2
	v_mov_b32_e32 v84, v2
	v_mov_b32_e32 v85, v2
	v_mov_b32_e32 v86, v2
	v_mov_b32_e32 v87, v2
	v_mov_b32_e32 v88, v2
	v_mov_b32_e32 v89, v2
	v_mov_b32_e32 v98, v2
	v_mov_b32_e32 v99, v2
	v_mov_b32_e32 v100, v2
	v_mov_b32_e32 v101, v2
	v_mov_b32_e32 v102, v2
	v_mov_b32_e32 v103, v2
	v_mov_b32_e32 v104, v2
	v_mov_b32_e32 v105, v2
	v_mov_b32_e32 v130, v2
	v_mov_b32_e32 v131, v2
	v_mov_b32_e32 v132, v2
	v_mov_b32_e32 v133, v2
	v_mov_b32_e32 v134, v2
	v_mov_b32_e32 v135, v2
	v_mov_b32_e32 v136, v2
	v_mov_b32_e32 v137, v2
	v_mov_b32_e32 v74, v2
	v_mov_b32_e32 v75, v2
	v_mov_b32_e32 v76, v2
	v_mov_b32_e32 v77, v2
	v_mov_b32_e32 v78, v2
	v_mov_b32_e32 v79, v2
	v_mov_b32_e32 v80, v2
	v_mov_b32_e32 v81, v2
	v_mov_b32_e32 v90, v2
	v_mov_b32_e32 v91, v2
	v_mov_b32_e32 v92, v2
	v_mov_b32_e32 v93, v2
	v_mov_b32_e32 v94, v2
	v_mov_b32_e32 v95, v2
	v_mov_b32_e32 v96, v2
	v_mov_b32_e32 v97, v2
	v_mov_b32_e32 v114, v2
	v_mov_b32_e32 v115, v2
	v_mov_b32_e32 v116, v2
	v_mov_b32_e32 v117, v2
	v_mov_b32_e32 v118, v2
	v_mov_b32_e32 v119, v2
	v_mov_b32_e32 v120, v2
	v_mov_b32_e32 v121, v2
	v_mov_b32_e32 v138, v2
	v_mov_b32_e32 v139, v2
	v_mov_b32_e32 v140, v2
	v_mov_b32_e32 v141, v2
	v_mov_b32_e32 v142, v2
	v_mov_b32_e32 v143, v2
	v_mov_b32_e32 v144, v2
	v_mov_b32_e32 v145, v2
	v_mov_b32_e32 v62, v2
	v_mov_b32_e32 v63, v2
	v_mov_b32_e32 v64, v2
	v_mov_b32_e32 v65, v2
	v_mov_b32_e32 v58, v2
	v_mov_b32_e32 v59, v2
	v_mov_b32_e32 v60, v2
	v_mov_b32_e32 v61, v2
	v_mov_b32_e32 v46, v2
	v_mov_b32_e32 v47, v2
	v_mov_b32_e32 v48, v2
	v_mov_b32_e32 v49, v2
	v_mov_b32_e32 v42, v2
	v_mov_b32_e32 v43, v2
	v_mov_b32_e32 v44, v2
	v_mov_b32_e32 v45, v2
	v_mov_b32_e32 v30, v2
	v_mov_b32_e32 v31, v2
	v_mov_b32_e32 v32, v2
	v_mov_b32_e32 v33, v2
	v_mov_b32_e32 v26, v2
	v_mov_b32_e32 v27, v2
	v_mov_b32_e32 v28, v2
	v_mov_b32_e32 v29, v2
	v_mov_b32_e32 v14, v2
	v_mov_b32_e32 v15, v2
	v_mov_b32_e32 v16, v2
	v_mov_b32_e32 v17, v2
	v_mov_b32_e32 v10, v2
	v_mov_b32_e32 v11, v2
	v_mov_b32_e32 v12, v2
	v_mov_b32_e32 v13, v2
	.p2align	3
	s_nop 0

.LBB0_2072:
	s_add_u32 s5, s26, 0x100
	s_addc_u32 s17, s27, 0
	s_add_u32 s18, s22, 0x100
	s_addc_u32 s19, s23, 0
	s_add_u32 s22, s22, 0x80
	s_addc_u32 s23, s23, 0
	s_mov_b32 s21, -2
	.p2align	3
